# v51 + nt on the DSA steady loop's selection-mask word loads (read-once stream)
# speedup vs baseline: 1.0100x; 1.0100x over previous
.LBB0_1077:
	v_lshl_add_u64 v[14:15], v[184:185], 0, s[54:55]
	s_mov_b64 s[38:39], 0xeb20000
	v_lshl_add_u64 v[2:3], v[14:15], 0, s[38:39]
	s_mov_b64 s[38:39], 0xeb28000
	v_add_u32_e32 v12, s29, v239
	v_lshl_add_u64 v[4:5], v[14:15], 0, s[38:39]
	global_load_dword v0, v[2:3], off nt
	global_load_dword v190, v[4:5], off nt
	global_load_dword v191, v[182:183], off offset:-4
	v_lshrrev_b32_e32 v2, v238, v211
	v_lshrrev_b32_e32 v3, v238, v213
	v_bfe_u32 v4, v2, 0, 4
	v_lshl_add_u32 v4, v4, 4, s100
	ds_read_b128 v[80:83], v4
	v_bfe_u32 v4, v2, 8, 4
	v_lshl_add_u32 v4, v4, 4, s100
	ds_read_b128 v[84:87], v4
	v_bfe_u32 v4, v2, 16, 4
	v_lshl_add_u32 v4, v4, 4, s100
	ds_read_b128 v[88:91], v4
	v_bfe_u32 v4, v2, 24, 4
	v_lshl_add_u32 v4, v4, 4, s100
	ds_read_b128 v[92:95], v4
	v_bfe_u32 v4, v3, 0, 4
	v_lshl_add_u32 v4, v4, 4, s100
	ds_read_b128 v[96:99], v4
	v_bfe_u32 v4, v3, 8, 4
	v_lshl_add_u32 v4, v4, 4, s100
	ds_read_b128 v[100:103], v4
	v_bfe_u32 v4, v3, 16, 4
	v_lshl_add_u32 v4, v4, 4, s100
	ds_read_b128 v[104:107], v4
	v_bfe_u32 v4, v3, 24, 4
	v_lshl_add_u32 v4, v4, 4, s100
	ds_read_b128 v[108:111], v4
	ds_read_b64_tr_b16 v[176:177], v12 offset:24576
	ds_read_b64_tr_b16 v[178:179], v12 offset:25088
	s_waitcnt lgkmcnt(6)
	v_mfma_f32_32x32x16_bf16 v[80:95], v[172:175], v[124:127], v[80:95]
	v_add_f32_e32 v2, v64, v65
	v_add_f32_e32 v2, v66, v2
	v_add_f32_e32 v2, v67, v2
	v_add_f32_e32 v2, v68, v2
	v_add_f32_e32 v2, v69, v2
	v_cvt_pk_bf16_f32 v140, v64, v65
	v_cvt_pk_bf16_f32 v141, v66, v67
	ds_read_b64_tr_b16 v[172:173], v12 offset:28672
	ds_read_b64_tr_b16 v[174:175], v12 offset:29184
	s_waitcnt lgkmcnt(4)
	v_mfma_f32_32x32x16_bf16 v[96:111], v[164:167], v[124:127], v[96:111]
	v_add_f32_e32 v2, v70, v2
	v_add_f32_e32 v2, v71, v2
	v_add_f32_e32 v2, v72, v2
	v_add_f32_e32 v2, v73, v2
	v_cvt_pk_bf16_f32 v142, v68, v69
	v_cvt_pk_bf16_f32 v143, v70, v71
	ds_read_b64_tr_b16 v[164:165], v12 offset:25600
	ds_read_b64_tr_b16 v[166:167], v12 offset:26112
	v_mfma_f32_32x32x16_bf16 v[80:95], v[168:171], v[120:123], v[80:95]
	v_add_f32_e32 v2, v74, v2
	v_add_f32_e32 v2, v75, v2
	v_add_f32_e32 v2, v76, v2
	v_add_f32_e32 v2, v77, v2
	v_cvt_pk_bf16_f32 v136, v72, v73
	v_cvt_pk_bf16_f32 v137, v74, v75
	ds_read_b64_tr_b16 v[168:169], v12 offset:29696
	ds_read_b64_tr_b16 v[170:171], v12 offset:30208
	v_mfma_f32_32x32x16_bf16 v[96:111], v[160:163], v[120:123], v[96:111]
	v_add_f32_e32 v2, v78, v2
	v_add_f32_e32 v2, v79, v2
	v_add_f32_e32 v2, v48, v2
	v_add_f32_e32 v2, v49, v2
	v_cvt_pk_bf16_f32 v138, v76, v77
	v_cvt_pk_bf16_f32 v139, v78, v79
	ds_read_b64_tr_b16 v[160:161], v12 offset:26624
	ds_read_b64_tr_b16 v[162:163], v12 offset:27136
	v_mfma_f32_32x32x16_bf16 v[80:95], v[156:159], v[116:119], v[80:95]
	v_add_f32_e32 v2, v50, v2
	v_add_f32_e32 v2, v51, v2
	v_add_f32_e32 v2, v52, v2
	v_add_f32_e32 v6, v53, v2
	v_cvt_pk_bf16_f32 v132, v48, v49
	v_cvt_pk_bf16_f32 v133, v50, v51
	ds_read_b64_tr_b16 v[2:3], v12 offset:30720
	ds_read_b64_tr_b16 v[4:5], v12 offset:31232
	v_mfma_f32_32x32x16_bf16 v[96:111], v[152:155], v[116:119], v[96:111]
	v_add_f32_e32 v6, v54, v6
	v_add_f32_e32 v6, v55, v6
	v_add_f32_e32 v6, v56, v6
	v_add_f32_e32 v10, v57, v6
	v_cvt_pk_bf16_f32 v134, v52, v53
	v_cvt_pk_bf16_f32 v135, v54, v55
	ds_read_b64_tr_b16 v[6:7], v12 offset:27648
	ds_read_b64_tr_b16 v[8:9], v12 offset:28160
	v_mfma_f32_32x32x16_bf16 v[80:95], v[148:151], v[112:115], v[80:95]
	v_add_f32_e32 v10, v58, v10
	v_add_f32_e32 v10, v59, v10
	v_add_f32_e32 v10, v60, v10
	v_add_f32_e32 v48, v61, v10
	v_cvt_pk_bf16_f32 v128, v56, v57
	v_cvt_pk_bf16_f32 v129, v58, v59
	ds_read_b64_tr_b16 v[10:11], v12 offset:31744
	ds_read_b64_tr_b16 v[12:13], v12 offset:32256
	v_mfma_f32_32x32x16_bf16 v[96:111], v[144:147], v[112:115], v[96:111]
	v_add_f32_e32 v48, v62, v48
	v_add_f32_e32 v48, v63, v48
	v_cvt_pk_bf16_f32 v130, v60, v61
	v_cvt_pk_bf16_f32 v131, v62, v63
	v_lshl_add_u64 v[186:187], v[216:217], 0, s[54:55]
	v_lshl_add_u64 v[50:51], v[186:187], 0, s[20:21]
	s_add_i32 s29, s59, s63
	s_mov_b32 m0, s29
	s_nop 0
	global_load_lds_dwordx4 v[50:51], off
	v_lshl_add_u64 v[188:189], v[218:219], 0, s[54:55]
	v_lshl_add_u64 v[50:51], v[188:189], 0, s[24:25]
	s_add_i32 s29, s57, s62
	s_mov_b32 m0, s29
	s_nop 0
	global_load_lds_dwordx4 v[50:51], off
	s_waitcnt vmcnt(7)
	v_mul_f32_e32 v49, v201, v209
	v_cmp_nge_f32_e32 vcc, s73, v49
	v_cmp_neq_f32_e64 s[38:39], 0, v207
	s_or_b64 vcc, vcc, s[38:39]
	s_cmp_lg_u64 vcc, 0
	s_cselect_b64 s[38:39], -1, 0
	s_cbranch_vccz .LBB0_1079
	v_sub_f32_e32 v95, v95, v207
	v_sub_f32_e32 v94, v94, v207
	v_sub_f32_e32 v93, v93, v207
	v_sub_f32_e32 v92, v92, v207
	v_sub_f32_e32 v91, v91, v207
	v_sub_f32_e32 v90, v90, v207
	v_sub_f32_e32 v89, v89, v207
	v_sub_f32_e32 v88, v88, v207
	v_sub_f32_e32 v87, v87, v207
	v_sub_f32_e32 v86, v86, v207
	v_sub_f32_e32 v85, v85, v207
	v_sub_f32_e32 v84, v84, v207
	v_sub_f32_e32 v83, v83, v207
	v_sub_f32_e32 v82, v82, v207
	v_sub_f32_e32 v81, v81, v207
	v_sub_f32_e32 v80, v80, v207
	v_sub_f32_e32 v111, v111, v207
	v_sub_f32_e32 v110, v110, v207
	v_sub_f32_e32 v109, v109, v207
	v_sub_f32_e32 v108, v108, v207
	v_sub_f32_e32 v107, v107, v207
	v_sub_f32_e32 v106, v106, v207
	v_sub_f32_e32 v105, v105, v207
	v_sub_f32_e32 v104, v104, v207
	v_sub_f32_e32 v103, v103, v207
	v_sub_f32_e32 v102, v102, v207
	v_sub_f32_e32 v101, v101, v207
	v_sub_f32_e32 v100, v100, v207
	v_sub_f32_e32 v99, v99, v207
	v_sub_f32_e32 v98, v98, v207
	v_sub_f32_e32 v97, v97, v207
	v_sub_f32_e32 v96, v96, v207

.LBB0_1082:
	s_add_i32 s29, s57, 0x2000
	s_cmpk_lg_i32 s57, 0x4000
	s_cselect_b32 s65, s29, 0
	s_mov_b64 s[38:39], 0xeb30000
	v_add_u32_e32 v12, s59, v239
	v_lshl_add_u64 v[2:3], v[14:15], 0, s[38:39]
	global_load_dword v192, v[2:3], off nt
	s_mov_b64 s[38:39], 0xeb38000
	v_lshl_add_u64 v[2:3], v[14:15], 0, s[38:39]
	global_load_dword v14, v[2:3], off nt
	global_load_dword v209, v[182:183], off
	v_lshrrev_b32_e32 v2, v238, v0
	v_lshrrev_b32_e32 v3, v238, v190
	v_bfe_u32 v4, v2, 0, 4
	v_lshl_add_u32 v4, v4, 4, s100
	ds_read_b128 v[80:83], v4
	v_bfe_u32 v4, v2, 8, 4
	v_lshl_add_u32 v4, v4, 4, s100
	ds_read_b128 v[84:87], v4
	v_bfe_u32 v4, v2, 16, 4
	v_lshl_add_u32 v4, v4, 4, s100
	ds_read_b128 v[88:91], v4
	v_bfe_u32 v4, v2, 24, 4
	v_lshl_add_u32 v4, v4, 4, s100
	ds_read_b128 v[92:95], v4
	v_bfe_u32 v4, v3, 0, 4
	v_lshl_add_u32 v4, v4, 4, s100
	ds_read_b128 v[96:99], v4
	v_bfe_u32 v4, v3, 8, 4
	v_lshl_add_u32 v4, v4, 4, s100
	ds_read_b128 v[100:103], v4
	v_bfe_u32 v4, v3, 16, 4
	v_lshl_add_u32 v4, v4, 4, s100
	ds_read_b128 v[104:107], v4
	v_bfe_u32 v4, v3, 24, 4
	v_lshl_add_u32 v4, v4, 4, s100
	ds_read_b128 v[108:111], v4
	ds_read_b64_tr_b16 v[156:157], v12 offset:24576
	ds_read_b64_tr_b16 v[158:159], v12 offset:25088
	s_waitcnt lgkmcnt(6)
	v_mfma_f32_32x32x16_bf16 v[80:95], v[140:143], v[124:127], v[80:95]
	v_add_f32_e32 v2, v64, v65
	v_add_f32_e32 v2, v66, v2
	v_add_f32_e32 v2, v67, v2
	v_add_f32_e32 v2, v68, v2
	v_add_f32_e32 v2, v69, v2
	v_cvt_pk_bf16_f32 v140, v64, v65
	v_cvt_pk_bf16_f32 v141, v66, v67
	ds_read_b64_tr_b16 v[152:153], v12 offset:28672
	ds_read_b64_tr_b16 v[154:155], v12 offset:29184
	s_waitcnt lgkmcnt(4)
	v_mfma_f32_32x32x16_bf16 v[96:111], v[136:139], v[124:127], v[96:111]
	v_add_f32_e32 v2, v70, v2
	v_add_f32_e32 v2, v71, v2
	v_add_f32_e32 v2, v72, v2
	v_add_f32_e32 v2, v73, v2
	v_cvt_pk_bf16_f32 v142, v68, v69
	v_cvt_pk_bf16_f32 v143, v70, v71
	ds_read_b64_tr_b16 v[144:145], v12 offset:25600
	ds_read_b64_tr_b16 v[146:147], v12 offset:26112
	v_mfma_f32_32x32x16_bf16 v[80:95], v[148:151], v[120:123], v[80:95]
	v_add_f32_e32 v2, v74, v2
	v_add_f32_e32 v2, v75, v2
	v_add_f32_e32 v2, v76, v2
	v_add_f32_e32 v2, v77, v2
	v_cvt_pk_bf16_f32 v136, v72, v73
	v_cvt_pk_bf16_f32 v137, v74, v75
	ds_read_b64_tr_b16 v[148:149], v12 offset:29696
	ds_read_b64_tr_b16 v[150:151], v12 offset:30208
	v_mfma_f32_32x32x16_bf16 v[96:111], v[176:179], v[120:123], v[96:111]
	v_add_f32_e32 v2, v78, v2
	v_add_f32_e32 v2, v79, v2
	v_add_f32_e32 v2, v48, v2
	v_add_f32_e32 v2, v49, v2
	v_cvt_pk_bf16_f32 v138, v76, v77
	v_cvt_pk_bf16_f32 v139, v78, v79
	ds_read_b64_tr_b16 v[176:177], v12 offset:26624
	ds_read_b64_tr_b16 v[178:179], v12 offset:27136
	v_mfma_f32_32x32x16_bf16 v[80:95], v[172:175], v[116:119], v[80:95]
	v_add_f32_e32 v2, v50, v2
	v_add_f32_e32 v2, v51, v2
	v_add_f32_e32 v2, v52, v2
	v_add_f32_e32 v6, v53, v2
	v_cvt_pk_bf16_f32 v132, v48, v49
	v_cvt_pk_bf16_f32 v133, v50, v51
	ds_read_b64_tr_b16 v[2:3], v12 offset:30720
	ds_read_b64_tr_b16 v[4:5], v12 offset:31232
	v_mfma_f32_32x32x16_bf16 v[96:111], v[164:167], v[116:119], v[96:111]
	v_add_f32_e32 v6, v54, v6
	v_add_f32_e32 v6, v55, v6
	v_add_f32_e32 v6, v56, v6
	v_add_f32_e32 v10, v57, v6
	v_cvt_pk_bf16_f32 v134, v52, v53
	v_cvt_pk_bf16_f32 v135, v54, v55
	ds_read_b64_tr_b16 v[6:7], v12 offset:27648
	ds_read_b64_tr_b16 v[8:9], v12 offset:28160
	v_mfma_f32_32x32x16_bf16 v[80:95], v[168:171], v[112:115], v[80:95]
	v_add_f32_e32 v10, v58, v10
	v_add_f32_e32 v10, v59, v10
	v_add_f32_e32 v10, v60, v10
	v_add_f32_e32 v15, v61, v10
	v_cvt_pk_bf16_f32 v128, v56, v57
	v_cvt_pk_bf16_f32 v129, v58, v59
	ds_read_b64_tr_b16 v[10:11], v12 offset:31744
	ds_read_b64_tr_b16 v[12:13], v12 offset:32256
	v_mfma_f32_32x32x16_bf16 v[96:111], v[160:163], v[112:115], v[96:111]
	v_add_f32_e32 v15, v62, v15
	v_add_f32_e32 v15, v63, v15
	v_cvt_pk_bf16_f32 v130, v60, v61
	v_cvt_pk_bf16_f32 v131, v62, v63
	v_lshl_add_u64 v[48:49], v[186:187], 0, s[22:23]
	s_add_i32 s29, s57, s63
	s_mov_b32 m0, s29
	s_nop 0
	global_load_lds_dwordx4 v[48:49], off
	v_lshl_add_u64 v[48:49], v[188:189], 0, s[70:71]
	s_add_i32 s29, s65, s62
	s_mov_b32 m0, s29
	s_nop 0
	global_load_lds_dwordx4 v[48:49], off
	s_waitcnt vmcnt(7)
	v_mul_f32_e32 v48, v201, v191
	v_cmp_nge_f32_e32 vcc, s73, v48
	v_cmp_neq_f32_e64 s[38:39], 0, v207
	s_or_b64 vcc, vcc, s[38:39]
	s_cmp_lg_u64 vcc, 0
	s_cselect_b64 s[38:39], -1, 0
	s_cbranch_vccz .LBB0_1084
	v_sub_f32_e32 v95, v95, v207
	v_sub_f32_e32 v94, v94, v207
	v_sub_f32_e32 v93, v93, v207
	v_sub_f32_e32 v92, v92, v207
	v_sub_f32_e32 v91, v91, v207
	v_sub_f32_e32 v90, v90, v207
	v_sub_f32_e32 v89, v89, v207
	v_sub_f32_e32 v88, v88, v207
	v_sub_f32_e32 v87, v87, v207
	v_sub_f32_e32 v86, v86, v207
	v_sub_f32_e32 v85, v85, v207
	v_sub_f32_e32 v84, v84, v207
	v_sub_f32_e32 v83, v83, v207
	v_sub_f32_e32 v82, v82, v207
	v_sub_f32_e32 v81, v81, v207
	v_sub_f32_e32 v80, v80, v207
	v_sub_f32_e32 v111, v111, v207
	v_sub_f32_e32 v110, v110, v207
	v_sub_f32_e32 v109, v109, v207
	v_sub_f32_e32 v108, v108, v207
	v_sub_f32_e32 v107, v107, v207
	v_sub_f32_e32 v106, v106, v207
	v_sub_f32_e32 v105, v105, v207
	v_sub_f32_e32 v104, v104, v207
	v_sub_f32_e32 v103, v103, v207
	v_sub_f32_e32 v102, v102, v207
	v_sub_f32_e32 v101, v101, v207
	v_sub_f32_e32 v100, v100, v207
	v_sub_f32_e32 v99, v99, v207
	v_sub_f32_e32 v98, v98, v207
	v_sub_f32_e32 v97, v97, v207
	v_sub_f32_e32 v96, v96, v207
